# DSA selection-mask rebuild in two load groups; LDS-write data in registers no later load targets, LDS writes drained before the second load group
# baseline (speedup 1.0000x reference)
.LBB0_1636:
	s_mov_b64 s[36:37], vcc
	s_and_saveexec_b64 s[10:11], vcc
	v_ashrrev_i32_e32 v90, 8, v20
	v_lshlrev_b32_e32 v90, 10, v90
	v_mov_b32_e32 v91, v3
	v_lshl_add_u64 v[90:91], v[4:5], 0, v[90:91]
	v_add_co_u32_e32 v98, vcc, 0x1000, v90
	s_nop 1
	v_addc_co_u32_e32 v99, vcc, 0, v91, vcc
	global_load_dwordx4 v[100:103], v[90:91], off
	global_load_dwordx4 v[104:107], v[90:91], off offset:2048
	global_load_dwordx4 v[108:111], v[98:99], off
	global_load_dwordx4 v[112:115], v[98:99], off offset:2048
	s_mov_b64 exec, s[10:11]
	s_and_saveexec_b64 s[10:11], s[36:37]
	v_ashrrev_i32_e32 v7, 6, v20
	v_lshlrev_b32_e32 v12, 4, v7
	s_movk_i32 s13, 0x104
	v_mad_u32_u24 v13, v7, s13, v6
	v_add_co_u32_e32 v90, vcc, 0x2000, v90
	s_nop 1
	v_addc_co_u32_e32 v91, vcc, 0, v91, vcc
	v_add_co_u32_e32 v98, vcc, 0x2000, v98
	s_nop 1
	v_addc_co_u32_e32 v99, vcc, 0, v99, vcc
	s_waitcnt vmcnt(0)
	v_lshrrev_b64 v[8:9], v12, v[100:101]
	v_lshrrev_b64 v[10:11], v12, v[102:103]
	v_and_b32_e32 v8, 0xffff, v8
	v_lshl_or_b32 v92, v10, 16, v8
	ds_write_b32 v13, v92 offset:0
	v_lshrrev_b64 v[8:9], v12, v[104:105]
	v_lshrrev_b64 v[10:11], v12, v[106:107]
	v_and_b32_e32 v8, 0xffff, v8
	v_lshl_or_b32 v93, v10, 16, v8
	ds_write_b32 v13, v93 offset:2080
	v_lshrrev_b64 v[8:9], v12, v[108:109]
	v_lshrrev_b64 v[10:11], v12, v[110:111]
	v_and_b32_e32 v8, 0xffff, v8
	v_lshl_or_b32 v94, v10, 16, v8
	ds_write_b32 v13, v94 offset:4160
	v_lshrrev_b64 v[8:9], v12, v[112:113]
	v_lshrrev_b64 v[10:11], v12, v[114:115]
	v_and_b32_e32 v8, 0xffff, v8
	v_lshl_or_b32 v95, v10, 16, v8
	ds_write_b32 v13, v95 offset:6240
	s_waitcnt lgkmcnt(0)
	global_load_dwordx4 v[100:103], v[90:91], off
	global_load_dwordx4 v[104:107], v[90:91], off offset:2048
	global_load_dwordx4 v[108:111], v[98:99], off
	global_load_dwordx4 v[112:115], v[98:99], off offset:2048
	s_waitcnt vmcnt(0)
	v_lshrrev_b64 v[8:9], v12, v[100:101]
	v_lshrrev_b64 v[10:11], v12, v[102:103]
	v_and_b32_e32 v8, 0xffff, v8
	v_lshl_or_b32 v92, v10, 16, v8
	ds_write_b32 v13, v92 offset:8320
	v_lshrrev_b64 v[8:9], v12, v[104:105]
	v_lshrrev_b64 v[10:11], v12, v[106:107]
	v_and_b32_e32 v8, 0xffff, v8
	v_lshl_or_b32 v93, v10, 16, v8
	ds_write_b32 v13, v93 offset:10400
	v_lshrrev_b64 v[8:9], v12, v[108:109]
	v_lshrrev_b64 v[10:11], v12, v[110:111]
	v_and_b32_e32 v8, 0xffff, v8
	v_lshl_or_b32 v94, v10, 16, v8
	ds_write_b32 v13, v94 offset:12480
	v_lshrrev_b64 v[8:9], v12, v[112:113]
	v_lshrrev_b64 v[10:11], v12, v[114:115]
	v_and_b32_e32 v8, 0xffff, v8
	v_lshl_or_b32 v95, v10, 16, v8
	ds_write_b32 v13, v95 offset:14560
	s_waitcnt lgkmcnt(0)
	s_mov_b64 exec, s[10:11]
